# v63 plus dcap W loads with default cache policy instead of nt (W is resident in the memory-side cache after the in-LSTM prefetch)
# speedup vs baseline: 1.0093x; 1.0068x over previous
.LBB4_2:
	s_or_b64 exec, exec, s[12:13]
	v_lshrrev_b32_e32 v101, 6, v0
	v_lshl_or_b32 v92, s2, 2, v101
	v_min_i32_e32 v104, 0x200, v92
	v_bfe_u32 v1, v0, 4, 2
	s_waitcnt vmcnt(10) lgkmcnt(0)
	v_mad_u64_u32 v[90:91], s[6:7], v92, 12, v[104:105]
	v_and_b32_e32 v106, 15, v0
	v_add_u32_e32 v2, v90, v1
	v_mul_u32_u24_e32 v98, 0x3200, v106
	v_ashrrev_i32_e32 v3, 31, v2
	v_lshl_add_u64 v[4:5], v[2:3], 0, v[98:99]
	v_lshlrev_b64 v[4:5], 5, v[4:5]
	v_lshl_add_u64 v[118:119], s[4:5], 0, v[4:5]
	s_movk_i32 s3, 0x1400
	v_mov_b64_e32 v[4:5], s[8:9]
	v_mad_i64_i32 v[2:3], s[6:7], v2, s3, v[4:5]
	v_lshlrev_b32_e32 v4, 3, v0
	v_and_b32_e32 v4, 0x78, v4
	v_lshlrev_b32_e32 v102, 2, v4
	v_mov_b32_e32 v103, v99
	v_lshl_add_u64 v[2:3], v[2:3], 0, v[102:103]
	global_load_dwordx4 v[74:77], v[2:3], off offset:16
	global_load_dwordx4 v[78:81], v[2:3], off
	global_load_dwordx4 v[66:69], v[2:3], off offset:528
	global_load_dwordx4 v[70:73], v[2:3], off offset:512
	global_load_dwordx4 v[58:61], v[2:3], off offset:1040
	global_load_dwordx4 v[62:65], v[2:3], off offset:1024
	global_load_dwordx4 v[46:49], v[2:3], off offset:1552
	global_load_dwordx4 v[54:57], v[2:3], off offset:1536
	global_load_dwordx4 v[38:41], v[2:3], off offset:2064
	global_load_dwordx4 v[50:53], v[2:3], off offset:2048
	global_load_dwordx4 v[34:37], v[2:3], off offset:2576
	global_load_dwordx4 v[42:45], v[2:3], off offset:2560
	global_load_dwordx4 v[14:17], v[2:3], off offset:3088
	global_load_dwordx4 v[30:33], v[2:3], off offset:3072
	global_load_dwordx4 v[6:9], v[2:3], off offset:3600
	global_load_dwordx4 v[18:21], v[2:3], off offset:3584
	s_movk_i32 s16, 0x1000
	s_mov_b64 s[6:7], 0x1000
	v_add_co_u32_e32 v120, vcc, s16, v2
	v_lshl_add_u64 v[4:5], v[2:3], 0, s[6:7]
	s_nop 0
	v_addc_co_u32_e32 v121, vcc, 0, v3, vcc
	s_mov_b64 s[12:13], 0x1200
	global_load_dwordx4 v[26:29], v[120:121], off
	global_load_dwordx4 v[10:13], v[4:5], off offset:16
	v_lshl_add_u64 v[122:123], v[2:3], 0, s[12:13]
	global_load_dwordx4 v[22:25], v[120:121], off offset:512
	global_load_dwordx4 v[2:5], v[122:123], off offset:16
	global_load_dwordx4 v[82:85], v[118:119], off offset:16
	global_load_dwordx4 v[86:89], v[118:119], off
	s_movk_i32 s18, 0x200
	s_mov_b32 s17, 0
	v_lshlrev_b32_e32 v100, 2, v0
	s_and_saveexec_b64 s[14:15], s[0:1]
	s_cbranch_execz .LBB4_4
	v_add_f32_e32 v91, 0, v93
	v_add_f32_e32 v91, v91, v94
	v_add_f32_e32 v91, v91, v95
	v_add_f32_e32 v91, v91, v96
	v_add_f32_e32 v91, v91, v97
	v_add_f32_e32 v91, v91, v105
	s_waitcnt vmcnt(31)
	v_add_f32_e32 v91, v91, v107
	s_waitcnt vmcnt(30)
	v_add_f32_e32 v91, v91, v108
	s_waitcnt vmcnt(29)
	v_add_f32_e32 v91, v91, v109
	s_waitcnt vmcnt(28)
	v_add_f32_e32 v91, v91, v110
	s_waitcnt vmcnt(27)
	v_add_f32_e32 v91, v91, v111
	s_waitcnt vmcnt(26)
	v_add_f32_e32 v91, v91, v112
	s_waitcnt vmcnt(25)
	v_add_f32_e32 v91, v91, v113
	s_waitcnt vmcnt(24)
	v_add_f32_e32 v91, v91, v114
	s_waitcnt vmcnt(23)
	v_add_f32_e32 v91, v91, v115
	s_waitcnt vmcnt(22)
	v_add_f32_e32 v91, v91, v116
	s_mov_b32 s0, 0xf800000
	v_mul_f32_e32 v93, 0x4f800000, v91
	v_cmp_gt_f32_e32 vcc, s0, v91
	s_nop 1
	v_cndmask_b32_e32 v93, v91, v93, vcc
	v_sqrt_f32_e32 v94, v93
	v_add_f32_e32 v91, 1.0, v91
	v_add_u32_e32 v95, -1, v94
	v_fma_f32 v96, -v95, v94, v93
	v_cmp_ge_f32_e64 s[0:1], 0, v96
	v_add_u32_e32 v96, 1, v94
	s_nop 0
	v_cndmask_b32_e64 v95, v94, v95, s[0:1]
	v_fma_f32 v94, -v96, v94, v93
	v_cmp_lt_f32_e64 s[0:1], 0, v94
	s_nop 1
	v_cndmask_b32_e64 v94, v95, v96, s[0:1]
	v_mul_f32_e32 v95, 0x37800000, v94
	v_cndmask_b32_e32 v94, v94, v95, vcc
	v_mov_b32_e32 v95, 0x260
	v_cmp_class_f32_e32 vcc, v93, v95
	s_nop 1
	v_cndmask_b32_e32 v93, v94, v93, vcc
	v_div_scale_f32 v94, s[0:1], v91, v91, v93
	v_rcp_f32_e32 v95, v94
	s_nop 0
	v_fma_f32 v96, -v94, v95, 1.0
	v_fmac_f32_e32 v95, v96, v95
	v_div_scale_f32 v96, vcc, v93, v91, v93
	v_mul_f32_e32 v97, v96, v95
	v_fma_f32 v103, -v94, v97, v96
	v_fmac_f32_e32 v97, v103, v95
	v_fma_f32 v94, -v94, v97, v96
	v_div_fmas_f32 v94, v94, v95, v97
	v_div_fixup_f32 v91, v94, v91, v93
	v_mul_f32_e32 v91, 0x45800000, v91
	v_lshlrev_b32_e32 v93, 2, v0
	ds_write_b32 v93, v91 offset:40960

.LBB4_5:
	v_mov_b32_e32 v112, v110
	v_mov_b32_e32 v113, v110
	v_add_u32_e32 v104, s17, v108
	v_mov_b32_e32 v111, v110
	v_mov_b64_e32 v[196:197], v[112:113]
	v_mov_b64_e32 v[200:201], v[112:113]
	v_mov_b64_e32 v[188:189], v[112:113]
	v_mov_b64_e32 v[180:181], v[112:113]
	v_mov_b64_e32 v[176:177], v[112:113]
	v_mov_b64_e32 v[168:169], v[112:113]
	v_mov_b64_e32 v[160:161], v[112:113]
	v_mov_b64_e32 v[152:153], v[112:113]
	v_mov_b64_e32 v[144:145], v[112:113]
	v_mov_b64_e32 v[136:137], v[112:113]
	v_mov_b64_e32 v[128:129], v[112:113]
	v_mov_b64_e32 v[120:121], v[112:113]
	v_mov_b64_e32 v[116:117], v[112:113]
	v_mov_b64_e32 v[124:125], v[112:113]
	v_mov_b64_e32 v[132:133], v[112:113]
	v_mov_b64_e32 v[140:141], v[112:113]
	v_mov_b64_e32 v[148:149], v[112:113]
	v_mov_b64_e32 v[156:157], v[112:113]
	v_mov_b64_e32 v[164:165], v[112:113]
	v_mov_b64_e32 v[172:173], v[112:113]
	v_mov_b64_e32 v[184:185], v[112:113]
	v_mov_b64_e32 v[192:193], v[112:113]
	v_cmp_lt_i32_e32 vcc, v104, v107
	v_mov_b64_e32 v[194:195], v[110:111]
	v_mov_b64_e32 v[198:199], v[110:111]
	v_mov_b64_e32 v[186:187], v[110:111]
	v_mov_b64_e32 v[178:179], v[110:111]
	v_mov_b64_e32 v[174:175], v[110:111]
	v_mov_b64_e32 v[166:167], v[110:111]
	v_mov_b64_e32 v[158:159], v[110:111]
	v_mov_b64_e32 v[150:151], v[110:111]
	v_mov_b64_e32 v[142:143], v[110:111]
	v_mov_b64_e32 v[134:135], v[110:111]
	v_mov_b64_e32 v[126:127], v[110:111]
	v_mov_b64_e32 v[118:119], v[110:111]
	v_mov_b64_e32 v[114:115], v[110:111]
	v_mov_b64_e32 v[122:123], v[110:111]
	v_mov_b64_e32 v[130:131], v[110:111]
	v_mov_b64_e32 v[138:139], v[110:111]
	v_mov_b64_e32 v[146:147], v[110:111]
	v_mov_b64_e32 v[154:155], v[110:111]
	v_mov_b64_e32 v[162:163], v[110:111]
	v_mov_b64_e32 v[170:171], v[110:111]
	v_mov_b64_e32 v[182:183], v[110:111]
	v_mov_b64_e32 v[190:191], v[110:111]
	s_and_saveexec_b64 s[0:1], vcc
	s_cbranch_execz .LBB4_7
	v_ashrrev_i32_e32 v105, 31, v104
	v_lshl_add_u64 v[112:113], v[104:105], 0, v[98:99]
	v_mad_i64_i32 v[104:105], s[8:9], v104, s3, v[102:103]
	global_load_dwordx4 v[114:117], v[104:105], off offset:16
	global_load_dwordx4 v[118:121], v[104:105], off
	global_load_dwordx4 v[122:125], v[104:105], off offset:528
	global_load_dwordx4 v[126:129], v[104:105], off offset:512
	global_load_dwordx4 v[130:133], v[104:105], off offset:1040
	global_load_dwordx4 v[134:137], v[104:105], off offset:1024
	global_load_dwordx4 v[138:141], v[104:105], off offset:1552
	global_load_dwordx4 v[142:145], v[104:105], off offset:1536
	global_load_dwordx4 v[146:149], v[104:105], off offset:2064
	global_load_dwordx4 v[150:153], v[104:105], off offset:2048
	global_load_dwordx4 v[154:157], v[104:105], off offset:2576
	global_load_dwordx4 v[158:161], v[104:105], off offset:2560
	global_load_dwordx4 v[162:165], v[104:105], off offset:3088
	global_load_dwordx4 v[166:169], v[104:105], off offset:3072
	global_load_dwordx4 v[170:173], v[104:105], off offset:3600
	global_load_dwordx4 v[174:177], v[104:105], off offset:3584
	v_add_co_u32_e32 v186, vcc, s16, v104
	v_lshlrev_b64 v[112:113], 5, v[112:113]
	v_lshl_add_u64 v[182:183], v[104:105], 0, s[6:7]
	v_addc_co_u32_e32 v187, vcc, 0, v105, vcc
	v_lshl_add_u64 v[112:113], s[4:5], 0, v[112:113]
	global_load_dwordx4 v[178:181], v[186:187], off
	s_nop 0
	global_load_dwordx4 v[182:185], v[182:183], off offset:16
	v_lshl_add_u64 v[104:105], v[104:105], 0, s[12:13]
	global_load_dwordx4 v[186:189], v[186:187], off offset:512
	s_nop 0
	global_load_dwordx4 v[190:193], v[104:105], off offset:16
	global_load_dwordx4 v[194:197], v[112:113], off offset:16
	global_load_dwordx4 v[198:201], v[112:113], off
